# router top-8 loop: next token's logits requested at the top of the trip; store of the atomic's returned rank deferred to the next trip (counted vmcnt(3)), so the load and the atomic round trip are no
# speedup vs baseline: 1.0040x; 1.0004x over previous
.LBB0_2801:
	s_lshl_b32 s2, s9, 3
	s_lshl_b32 s0, s9, 7
	s_and_b32 s0, s0, 0xfffff000
	s_and_b32 s1, s2, 0xf8
	s_or_b32 s3, s0, s1
	s_add_i32 s4, s0, 0x1000
	s_cmpk_eq_i32 s12, 0x100
	s_cselect_b64 s[8:9], -1, 0
	s_and_b64 s[0:1], s[8:9], exec
	s_cselect_b32 s0, s3, s2
	s_cselect_b32 s30, s4, 0x8000
	s_add_i32 s52, s0, s90
	s_cmp_ge_i32 s52, s30
	s_cbranch_scc1 .LBB0_2818
	v_readlane_b32 s2, v254, 43
	v_readlane_b32 s3, v254, 44
	s_mov_b32 s3, s11
	v_readlane_b32 s36, v252, 36
	s_lshl_b32 s12, s12, 3
	s_lshl_b64 s[0:1], s[2:3], 10
	v_readlane_b32 s38, v252, 38
	s_waitcnt vmcnt(0)
	v_lshlrev_b32_e32 v8, 2, v0
	v_readlane_b32 s39, v252, 39
	s_add_u32 s0, s38, s0
	v_ashrrev_i32_e32 v9, 31, v8
	s_addc_u32 s1, s39, s1
	v_lshlrev_b64 v[10:11], 2, v[8:9]
	v_lshl_add_u64 v[4:5], s[0:1], 0, v[10:11]
	global_load_dwordx4 v[4:7], v[4:5], off
	s_mov_b32 s0, s2
	v_writelane_b32 v254, s0, 43
	v_lshl_add_u64 v[10:11], s[28:29], 0, v[10:11]
	v_readlane_b32 s37, v252, 37
	v_writelane_b32 v254, s1, 44
	s_lshl_b32 s0, s2, 8
	s_mov_b32 s1, s11
	s_lshl_b64 s[0:1], s[0:1], 2
	s_add_u32 s0, s28, s0
	s_addc_u32 s1, s29, s1
	s_add_u32 s0, s0, 0x10000
	s_mov_b64 s[2:3], 0x77dc8000
	s_addc_u32 s1, s1, 0
	v_lshl_add_u64 v[10:11], v[10:11], 0, s[2:3]
	v_readlane_b32 s2, v254, 10
	v_readlane_b32 s40, v252, 40
	v_readlane_b32 s41, v252, 41
	v_add_u32_e32 v13, s2, v8
	s_add_u32 s2, s28, 0x7adc8000
	s_addc_u32 s3, s29, 0
	s_add_u32 s4, s28, 0x7aec8000
	s_addc_u32 s5, s29, 0
	s_add_u32 s6, s28, 0x7afc8000
	s_addc_u32 s7, s29, 0
	v_readlane_b32 s42, v252, 42
	v_readlane_b32 s43, v252, 43
	v_readlane_b32 s44, v252, 44
	v_readlane_b32 s45, v252, 45
	v_readlane_b32 s46, v252, 46
	v_readlane_b32 s47, v252, 47
	v_readlane_b32 s48, v252, 48
	v_readlane_b32 s49, v252, 49
	v_readlane_b32 s50, v252, 50
	v_readlane_b32 s51, v252, 51
	v_ashrrev_i32_e32 v12, 3, v0
	s_and_b64 s[8:9], s[8:9], exec
	v_cmp_gt_i32_e64 s[34:35], 8, v0
	v_ashrrev_i32_e32 v1, 31, v0
	s_cselect_b32 s28, 0x100, s12
	v_xor_b32_e32 v2, 4, v8
	v_xor_b32_e32 v9, 8, v8
	v_xor_b32_e32 v14, 16, v8
	v_cmp_lt_i32_e64 s[36:37], 0, v12
	v_cmp_lt_i32_e64 s[38:39], 1, v12
	v_cmp_lt_i32_e64 s[40:41], 2, v12
	v_cmp_lt_i32_e64 s[42:43], 3, v12
	v_cmp_lt_i32_e64 s[44:45], 4, v12
	v_cmp_lt_i32_e64 s[46:47], 5, v12
	v_cmp_lt_i32_e64 s[48:49], 6, v12
	v_cmp_lt_i32_e64 s[50:51], 7, v12
	v_or_b32_e32 v15, 1, v8
	v_or_b32_e32 v16, 2, v8
	v_or_b32_e32 v17, 3, v8
	v_add_u32_e32 v18, 0x400, v13
	s_ashr_i32 s53, s52, 31
	s_lshl_b64 s[8:9], s[52:53], 10
	v_lshl_add_u64 v[44:45], v[10:11], 0, s[8:9]
	global_load_dwordx4 v[40:43], v[44:45], off
	s_mov_b32 s100, 0
	s_waitcnt vmcnt(0)
	s_branch .LBB0_2804
.LBB0_2803:
	s_or_b64 exec, exec, s[8:9]
	s_waitcnt vmcnt(3)
	s_add_i32 s52, s52, s28
	s_cmp_ge_i32 s52, s30
	s_cbranch_scc1 .Lmy_rt_flush
.LBB0_2804:
	s_ashr_i32 s53, s52, 31
	s_lshl_b64 s[8:9], s[52:53], 10
	v_lshl_add_u64 v[12:13], v[10:11], 0, s[8:9]
	v_mul_f32_e32 v12, 0xbfb8aa3b, v40
	v_exp_f32_e32 v12, v12
	s_nop 0
	v_add_f32_e32 v12, 1.0, v12
	v_div_scale_f32 v13, s[8:9], v12, v12, 1.0
	v_rcp_f32_e32 v19, v13
	s_waitcnt lgkmcnt(0)
	v_fma_f32 v20, -v13, v19, 1.0
	v_fmac_f32_e32 v19, v20, v19
	v_div_scale_f32 v20, vcc, 1.0, v12, 1.0
	v_mul_f32_e32 v21, v20, v19
	v_fma_f32 v22, -v13, v21, v20
	v_fmac_f32_e32 v21, v22, v19
	v_fma_f32 v13, -v13, v21, v20
	v_div_fmas_f32 v13, v13, v19, v21
	v_div_fixup_f32 v12, v13, v12, 1.0
	v_mul_f32_e32 v13, 0xbfb8aa3b, v41
	v_exp_f32_e32 v13, v13
	v_add_f32_e32 v21, v4, v12
	v_add_f32_e32 v13, 1.0, v13
	v_div_scale_f32 v19, s[8:9], v13, v13, 1.0
	v_rcp_f32_e32 v20, v19
	s_nop 0
	v_fma_f32 v22, -v19, v20, 1.0
	v_fmac_f32_e32 v20, v22, v20
	v_div_scale_f32 v22, vcc, 1.0, v13, 1.0
	v_mul_f32_e32 v23, v22, v20
	v_fma_f32 v26, -v19, v23, v22
	v_fmac_f32_e32 v23, v26, v20
	v_fma_f32 v19, -v19, v23, v22
	v_div_fmas_f32 v19, v19, v20, v23
	v_div_fixup_f32 v13, v19, v13, 1.0
	v_mul_f32_e32 v19, 0xbfb8aa3b, v42
	v_exp_f32_e32 v19, v19
	v_add_f32_e32 v22, v5, v13
	v_add_f32_e32 v19, 1.0, v19
	v_div_scale_f32 v20, s[8:9], v19, v19, 1.0
	v_rcp_f32_e32 v23, v20
	s_nop 0
	v_fma_f32 v24, -v20, v23, 1.0
	v_fmac_f32_e32 v23, v24, v23
	v_div_scale_f32 v24, vcc, 1.0, v19, 1.0
	v_mul_f32_e32 v26, v24, v23
	v_fma_f32 v27, -v20, v26, v24
	v_fmac_f32_e32 v26, v27, v23
	v_fma_f32 v20, -v20, v26, v24
	v_div_fmas_f32 v20, v20, v23, v26
	v_div_fixup_f32 v19, v20, v19, 1.0
	v_mul_f32_e32 v20, 0xbfb8aa3b, v43
	s_add_i32 s12, s52, s28
	s_cmp_lt_i32 s12, s30
	s_cselect_b32 s12, s12, s52
	s_ashr_i32 s13, s12, 31
	s_lshl_b64 s[12:13], s[12:13], 10
	v_lshl_add_u64 v[44:45], v[10:11], 0, s[12:13]
	global_load_dwordx4 v[40:43], v[44:45], off
	v_exp_f32_e32 v20, v20
	v_add_f32_e32 v23, v6, v19
	v_add_f32_e32 v20, 1.0, v20
	v_div_scale_f32 v24, s[8:9], v20, v20, 1.0
	v_rcp_f32_e32 v25, v24
	s_mov_b32 s8, 0
	v_fma_f32 v26, -v24, v25, 1.0
	v_fmac_f32_e32 v25, v26, v25
	v_div_scale_f32 v26, vcc, 1.0, v20, 1.0
	v_mul_f32_e32 v27, v26, v25
	v_fma_f32 v28, -v24, v27, v26
	v_fmac_f32_e32 v27, v28, v25
	v_fma_f32 v24, -v24, v27, v26
	v_div_fmas_f32 v24, v24, v25, v27
	v_div_fixup_f32 v20, v24, v20, 1.0
	v_add_f32_e32 v25, v7, v20
	v_max_f32_e32 v24, v21, v22
	v_max_f32_e32 v27, v23, v25
	v_min_f32_e32 v26, v21, v22
	v_min_f32_e32 v28, v23, v25
	v_max_f32_e32 v29, v24, v27
	v_min_f32_e32 v24, v24, v27
	v_max3_f32 v24, v24, v26, v28
	ds_bpermute_b32 v26, v2, v29
	ds_bpermute_b32 v27, v2, v24
	s_waitcnt lgkmcnt(1)
	v_max_f32_e32 v26, v26, v26
	v_max_f32_e32 v28, v29, v26
	v_min_f32_e32 v26, v29, v26
	s_waitcnt lgkmcnt(0)
	v_max3_f32 v24, v26, v24, v27
	ds_bpermute_b32 v26, v9, v28
	ds_bpermute_b32 v27, v9, v24
	s_waitcnt lgkmcnt(1)
	v_max_f32_e32 v26, v26, v26
	v_max_f32_e32 v29, v28, v26
	v_min_f32_e32 v26, v28, v26
	s_waitcnt lgkmcnt(0)
	v_max3_f32 v24, v26, v24, v27
	ds_bpermute_b32 v26, v14, v29
	ds_bpermute_b32 v27, v14, v24
	s_waitcnt lgkmcnt(1)
	v_max_f32_e32 v26, v26, v26
	v_max_f32_e32 v28, v29, v26
	v_min_f32_e32 v26, v29, v26
	s_waitcnt lgkmcnt(0)
	v_max3_f32 v24, v26, v24, v27
	v_add_f32_e32 v24, v28, v24
	s_nop 0
	v_readlane_b32 s9, v24, 0
	s_nop 1
	v_cmp_eq_f32_e64 s[54:55], s9, v24
	v_cmp_gt_f32_e32 vcc, s9, v24
	s_and_b64 s[12:13], s[36:37], s[54:55]
	v_readlane_b32 s9, v24, 8
	s_or_b64 s[12:13], vcc, s[12:13]
	v_cndmask_b32_e64 v26, 0, 1, s[12:13]
	v_cmp_eq_f32_e64 s[54:55], s9, v24
	v_cmp_gt_f32_e32 vcc, s9, v24
	s_and_b64 s[12:13], s[38:39], s[54:55]
	v_readlane_b32 s9, v24, 16
	s_or_b64 s[12:13], vcc, s[12:13]
	v_cndmask_b32_e64 v27, 0, 1, s[12:13]
	v_cmp_eq_f32_e64 s[54:55], s9, v24
	v_cmp_gt_f32_e32 vcc, s9, v24
	s_and_b64 s[12:13], s[40:41], s[54:55]
	v_readlane_b32 s9, v24, 24
	s_or_b64 s[12:13], vcc, s[12:13]
	v_add_u32_e32 v26, v26, v27
	v_cmp_eq_f32_e64 s[54:55], s9, v24
	v_cndmask_b32_e64 v27, 0, 1, s[12:13]
	v_cmp_gt_f32_e32 vcc, s9, v24
	s_and_b64 s[12:13], s[42:43], s[54:55]
	v_readlane_b32 s9, v24, 32
	s_or_b64 s[12:13], vcc, s[12:13]
	v_cndmask_b32_e64 v28, 0, 1, s[12:13]
	v_cmp_eq_f32_e64 s[54:55], s9, v24
	v_cmp_gt_f32_e32 vcc, s9, v24
	s_and_b64 s[12:13], s[44:45], s[54:55]
	v_readlane_b32 s9, v24, 40
	s_or_b64 s[12:13], vcc, s[12:13]
	v_add3_u32 v26, v26, v27, v28
	v_cmp_eq_f32_e64 s[54:55], s9, v24
	v_cndmask_b32_e64 v27, 0, 1, s[12:13]
	v_cmp_gt_f32_e32 vcc, s9, v24
	s_and_b64 s[12:13], s[46:47], s[54:55]
	v_readlane_b32 s9, v24, 48
	s_or_b64 s[12:13], vcc, s[12:13]
	v_cndmask_b32_e64 v28, 0, 1, s[12:13]
	v_cmp_eq_f32_e64 s[54:55], s9, v24
	v_cmp_gt_f32_e32 vcc, s9, v24
	s_and_b64 s[12:13], s[48:49], s[54:55]
	v_readlane_b32 s9, v24, 56
	s_or_b64 s[12:13], vcc, s[12:13]
	v_add3_u32 v26, v26, v27, v28
	v_cmp_eq_f32_e64 s[54:55], s9, v24
	v_cndmask_b32_e64 v27, 0, 1, s[12:13]
	v_cmp_gt_f32_e32 vcc, s9, v24
	s_and_b64 s[12:13], s[50:51], s[54:55]
	s_or_b64 s[12:13], vcc, s[12:13]
	v_cndmask_b32_e64 v24, 0, 1, s[12:13]
	v_add3_u32 v24, v26, v27, v24
	v_cmp_gt_u32_e32 vcc, 4, v24
	v_mov_b32_e32 v27, 0xf149f2ca
	s_mov_b32 s9, 31
	v_cndmask_b32_e32 v21, v27, v21, vcc
	v_cndmask_b32_e32 v26, v27, v23, vcc
	v_not_b32_e32 v23, v21
	v_or_b32_e32 v24, 0x80000000, v21
	v_cmp_gt_i32_e64 s[54:55], 0, v21
	v_cndmask_b32_e32 v22, v27, v22, vcc
	s_nop 0
	v_cndmask_b32_e64 v21, v24, v23, s[54:55]
	v_cndmask_b32_e32 v24, 0, v21, vcc
	v_not_b32_e32 v21, v22
	v_or_b32_e32 v23, 0x80000000, v22
	v_cmp_gt_i32_e64 s[54:55], 0, v22
	v_or_b32_e32 v22, 0x80000000, v26
	s_nop 0
	v_cndmask_b32_e64 v21, v23, v21, s[54:55]
	v_cndmask_b32_e32 v23, 0, v21, vcc
	v_not_b32_e32 v21, v26
	v_cmp_gt_i32_e64 s[54:55], 0, v26
	s_nop 1
	v_cndmask_b32_e64 v21, v22, v21, s[54:55]
	v_cndmask_b32_e32 v22, 0, v21, vcc
	v_cndmask_b32_e32 v21, v27, v25, vcc
	v_not_b32_e32 v25, v21
	v_cmp_gt_i32_e64 s[54:55], 0, v21
	s_nop 1
	v_cndmask_b32_e64 v21, -|v21|, v25, s[54:55]
	v_cndmask_b32_e32 v21, 0, v21, vcc

.LBB0_2814:
	s_or_b64 exec, exec, s[12:13]
	s_waitcnt lgkmcnt(0)
	v_mov_b32_e32 v13, 0
	v_mov_b32_e32 v12, 0
	s_and_saveexec_b64 s[8:9], s[34:35]
	ds_read2_b32 v[12:13], v18 offset1:8
	s_or_b64 exec, exec, s[8:9]
	s_waitcnt lgkmcnt(0)
	ds_bpermute_b32 v19, v2, v13
	s_waitcnt lgkmcnt(0)
	s_waitcnt lgkmcnt(0)
	v_add_f32_e32 v19, v13, v19
	ds_bpermute_b32 v20, v9, v19
	s_waitcnt lgkmcnt(0)
	v_add_f32_e32 v19, v19, v20
	ds_bpermute_b32 v20, v14, v19
	s_and_saveexec_b64 s[8:9], s[34:35]
	s_cbranch_execz .LBB0_2803
	s_waitcnt lgkmcnt(0)
	v_add_f32_e32 v19, v19, v20
	v_div_scale_f32 v20, s[12:13], v19, v19, v13
	v_rcp_f32_e32 v21, v20
	v_div_scale_f32 v22, vcc, v13, v19, v13
	v_fma_f32 v23, -v20, v21, 1.0
	v_fmac_f32_e32 v21, v23, v21
	v_mul_f32_e32 v23, v22, v21
	v_fma_f32 v24, -v20, v23, v22
	v_fmac_f32_e32 v23, v24, v21
	v_fma_f32 v20, -v20, v23, v22
	v_div_fmas_f32 v20, v20, v21, v23
	v_div_fixup_f32 v19, v20, v19, v13
	v_ashrrev_i32_e32 v13, 31, v12
	v_lshl_add_u64 v[20:21], v[12:13], 2, s[0:1]
	s_cmp_eq_u32 s100, 0
	s_cbranch_scc1 .Lmy_rt_nopend
	s_waitcnt vmcnt(3)
	global_store_dword v[46:47], v48, off
.Lmy_rt_nopend:
	s_mov_b32 s100, 1
	global_atomic_add v48, v[20:21], v200, off sc0
	v_lshl_add_u64 v[20:21], s[52:53], 3, v[0:1]
	v_lshlrev_b64 v[20:21], 2, v[20:21]
	v_lshl_add_u64 v[22:23], s[2:3], 0, v[20:21]
	v_mul_f32_e32 v19, 0x40200000, v19
	global_store_dword v[22:23], v12, off
	v_lshl_add_u64 v[12:13], s[4:5], 0, v[20:21]
	global_store_dword v[12:13], v19, off
	v_lshl_add_u64 v[46:47], s[6:7], 0, v[20:21]
	s_branch .LBB0_2803
.Lmy_rt_flush:
	s_waitcnt vmcnt(0)
	s_and_saveexec_b64 s[8:9], s[34:35]
	global_store_dword v[46:47], v48, off
	s_or_b64 exec, exec, s[8:9]
